# t8_tailfirst
# baseline (speedup 1.0000x reference)
_Z11align_fusedPKfS0_PKiPf:
	s_load_dwordx2 s[6:7], s[0:1], 0x0
	s_sub_u32 s3, 0x1fff, s2
	s_sub_u32 s5, s2, 0xa00
	s_cmp_lt_u32 s2, 0xa00
	s_cselect_b32 s2, s3, s5
	s_mul_hi_u32 s3, s2, 0x1770
	s_mulk_i32 s2, 0x1770
	s_lshl_b64 s[4:5], s[2:3], 2
	s_waitcnt lgkmcnt(0)
	s_add_u32 s2, s6, s4
	s_addc_u32 s3, s7, s5
	v_mov_b32_e32 v31, 0
	v_lshlrev_b32_e32 v30, 4, v0
	v_lshl_add_u64 v[10:11], s[2:3], 0, v[30:31]
	s_movk_i32 s7, 0x2000
	v_add_co_u32_e32 v12, vcc, s7, v10
	s_movk_i32 s7, 0x3000
	s_nop 0
	v_addc_co_u32_e32 v13, vcc, 0, v11, vcc
	v_add_co_u32_e32 v18, vcc, s7, v10
	s_movk_i32 s6, 0xdc
	s_nop 0
	v_addc_co_u32_e32 v19, vcc, 0, v11, vcc
	v_add_co_u32_e32 v20, vcc, 0x4000, v10
	v_or_b32_e32 v48, 0x400, v0
	s_nop 0
	v_addc_co_u32_e32 v21, vcc, 0, v11, vcc
	v_or_b32_e32 v1, 0x500, v0
	v_cmp_gt_u32_e32 vcc, s6, v0
	global_load_dwordx4 v[2:5], v[12:13], off offset:-4096 nt
	global_load_dwordx4 v[6:9], v[12:13], off nt
	v_cndmask_b32_e32 v1, v48, v1, vcc
	global_load_dwordx4 v[10:13], v[18:19], off nt
	global_load_dwordx4 v[14:17], v[20:21], off nt
	v_lshlrev_b32_e32 v49, 4, v1
	global_load_dwordx4 v[22:25], v30, s[2:3] nt
	global_load_dwordx4 v[18:21], v49, s[2:3] nt
	v_and_b32_e32 v29, 63, v0
	v_cmp_gt_u32_e32 vcc, 64, v0
	v_mov_b32_e32 v26, v31
	v_mov_b32_e32 v27, v31
	v_mov_b32_e32 v28, v31
	s_and_saveexec_b64 s[2:3], vcc
	s_cbranch_execz .LBB0_2
	s_load_dwordx4 s[8:11], s[0:1], 0x8
	v_mul_u32_u24_e32 v1, 3, v29
	v_lshlrev_b32_e32 v31, 2, v29
	v_lshlrev_b32_e32 v1, 2, v1
	s_waitcnt lgkmcnt(0)
	global_load_dword v32, v31, s[10:11]
	global_load_dwordx3 v[26:28], v1, s[8:9] nt
	s_waitcnt vmcnt(1)
	v_lshl_add_u32 v31, v32, 1, v32
